# P10 grouped GEMM: next-unit row-table loads issued together with the gather-offset loads, one VMEM drain per unit instead of two
# speedup vs baseline: 1.0053x; 1.0052x over previous
; #define LAS __attribute__((address_space(3)))
;     __device__ __forceinline__ bool next(int i, Unit& u) const { if (i >= ncol) return false; u.pm = pm; u.pn = i; u.B = Bt + (size_t)i * BM * K * 2; u.e = 0; u.cnt = 0; u.off = 0; return true; }
;     ...
;         const bool has_next = S.next(ui + 1, nxt);
;         if constexpr (GATHER) {
;             unsigned vn[2][2];
;             if (has_next) S.avoff(nxt, Rr, Cc, vn, tid);
;             else {
; #pragma unroll
;                 for (int h = 0; h < 2; ++h)
; #pragma unroll
;                     for (int i = 0; i < 2; ++i) vn[h][i] = vc[h][i];
;             }
;             *(LAS u32x4*)vnslot = (u32x4){vn[0][0], vn[0][1], vn[1][0], vn[1][1]};
;             if (has_next) S.rowtab(nxt, rowtab + 512 * ((ui + 1) % 3), tid);
;         }
;     __device__ __forceinline__ void rowtab(const Unit& u, LAS unsigned* t, int tid) const {
;         if (tid < BM) { int r = u.pm * BM + tid; if (r >= u.cnt) r = u.cnt - 1; t[tid] = (unsigned)slot_ent[u.off + r]; t[BM + tid] = __float_as_uint(slot_w[u.off + r]); }
;     }
;     __device__ __forceinline__ void avoff(const Unit& u, const int (&)[2], const int (&)[2], unsigned (&v)[2][2], int tidq) const {
;         int R[2], C[2]; asm volatile("" : "+v"(tidq));
; #pragma unroll
;         for (int i = 0; i < 2; ++i) stage_rc(tidq * 16 + i * 8192, R[i], C[i]);
; #pragma unroll
;         for (int h = 0; h < 2; ++h)
; #pragma unroll
;             for (int i = 0; i < 2; ++i) {
;                 int r = u.pm * BM + h * HALF + R[i]; if (r >= u.cnt) r = u.cnt - 1;
;                 const int slot = u.off + r;
;                 const int row = TOKROWS ? (slot_ent[slot] >> 3) : slot;
;                 v[h][i] = (unsigned)(row * K + C[i] * 2);
;             }
.LBB0_597:
	v_cndmask_b32_e64 v0, 0, 1, s[6:7]
	v_cmp_ne_u32_e64 s[10:11], 1, v0
	s_andn2_b64 vcc, exec, s[6:7]
	v_add_u32_e32 v6, -1, v246
	v_mov_b32_e32 v3, v208
	v_mov_b32_e32 v2, v172
	v_mov_b32_e32 v1, v206
	v_mov_b32_e32 v0, v170
	v_mov_b64_e32 v[204:205], v[4:5]
	s_cbranch_vccnz .LBB0_599
	v_mov_b32_e32 v0, v231
	v_lshlrev_b32_e32 v3, 8, v248
	v_ashrrev_i32_e32 v2, 31, v0
	v_lshrrev_b32_e32 v2, 26, v2
	v_lshlrev_b32_e32 v1, 4, v0
	v_add_u32_e32 v2, v0, v2
	v_bfe_i32 v0, v0, 27, 1
	v_lshrrev_b32_e32 v0, 22, v0
	v_add_u32_e32 v0, v1, v0
	v_and_b32_e32 v0, 0xfffffc00, v0
	v_sub_u32_e32 v0, v1, v0
	v_ashrrev_i32_e32 v7, 6, v2
	v_lshrrev_b32_e32 v2, 4, v0
	v_bitop3_b32 v10, v2, v0, 32 bitop3:0x6c
	v_ashrrev_i32_e32 v2, 31, v10
	v_lshrrev_b32_e32 v2, 26, v2
	v_lshlrev_b32_e32 v0, 3, v7
	v_add_u32_e32 v11, v10, v2
	v_and_b32_e32 v0, -16, v0
	v_ashrrev_i32_e32 v2, 6, v11
	v_add_u32_e32 v2, v2, v0
	v_add_u32_e32 v0, 0x2000, v1
	v_ashrrev_i32_e32 v1, 31, v0
	v_lshrrev_b32_e32 v1, 22, v1
	v_add_u32_e32 v1, v0, v1
	v_ashrrev_i32_e32 v12, 10, v1
	v_mul_i32_i24_e32 v1, 0x400, v12
	v_sub_u32_e32 v0, v0, v1
	v_lshrrev_b32_e32 v1, 4, v0
	v_bitop3_b32 v13, v1, v0, 32 bitop3:0x6c
	v_ashrrev_i32_e32 v1, 31, v13
	v_lshrrev_b32_e32 v1, 26, v1
	v_lshlrev_b32_e32 v0, 3, v12
	v_add_u32_e32 v14, v13, v1
	v_and_b32_e32 v0, -16, v0
	v_ashrrev_i32_e32 v1, 6, v14
	v_add_u32_e32 v8, v1, v0
	v_add_u32_e32 v0, v2, v3
	v_min_i32_e32 v0, v0, v6
	v_add_u32_e32 v0, v0, v247
	v_ashrrev_i32_e32 v1, 31, v0
	v_lshl_add_u64 v[0:1], v[0:1], 2, s[22:23]
	v_or_b32_e32 v9, 0x80, v3
	global_load_dword v15, v[0:1], off
	v_add_u32_e32 v0, v8, v3
	v_add_u32_e32 v2, v2, v9
	v_min_i32_e32 v0, v0, v6
	v_min_i32_e32 v2, v2, v6
	v_add_u32_e32 v8, v8, v9
	v_add_u32_e32 v0, v0, v247
	v_add_u32_e32 v2, v2, v247
	v_min_i32_e32 v8, v8, v6
	v_ashrrev_i32_e32 v1, 31, v0
	v_ashrrev_i32_e32 v3, 31, v2
	v_add_u32_e32 v8, v8, v247
	v_lshl_add_u64 v[0:1], v[0:1], 2, s[22:23]
	v_lshl_add_u64 v[2:3], v[2:3], 2, s[22:23]
	v_ashrrev_i32_e32 v9, 31, v8
	v_lshl_add_u64 v[8:9], v[8:9], 2, s[22:23]
	global_load_dword v1, v[0:1], off
	s_nop 0
	global_load_dword v2, v[2:3], off
	s_nop 0
	global_load_dword v3, v[8:9], off
	v_and_b32_e32 v8, 0xc0, v11
	v_sub_u32_e32 v8, v10, v8
	v_lshlrev_b32_e32 v0, 5, v7
	v_ashrrev_i16_sdwa v8, v233, sext(v8) dst_sel:DWORD dst_unused:UNUSED_PAD src0_sel:DWORD src1_sel:BYTE_0
	v_and_b32_e32 v9, 0xc0, v14
	v_and_b32_e32 v0, 32, v0
	v_bfe_i32 v8, v8, 0, 16
	v_sub_u32_e32 v9, v13, v9
	v_lshlrev_b32_e32 v7, 5, v12
	v_add_lshl_u32 v8, v0, v8, 1
	v_ashrrev_i16_sdwa v0, v233, sext(v9) dst_sel:DWORD dst_unused:UNUSED_PAD src0_sel:DWORD src1_sel:BYTE_0
	v_and_b32_e32 v7, 32, v7
	v_bfe_i32 v0, v0, 0, 16
	v_add_lshl_u32 v7, v7, v0, 1
	v_mov_b64_e32 v[204:205], s[50:51]
	s_mov_b64 s[100:101], exec
	s_andn2_b64 exec, exec, s[8:9]
	s_cbranch_execz .Lp10_rt_skip
	v_lshl_add_u32 v20, v248, 8, v231
	v_min_i32_e32 v20, v20, v6
	v_add_u32_e32 v20, v20, v247
	v_ashrrev_i32_e32 v21, 31, v20
	v_lshlrev_b64 v[20:21], 2, v[20:21]
	v_lshl_add_u64 v[22:23], s[22:23], 0, v[20:21]
	v_lshl_add_u64 v[20:21], s[24:25], 0, v[20:21]
	global_load_dword v22, v[22:23], off
	s_nop 0
	global_load_dword v20, v[20:21], off
.Lp10_rt_skip:
	s_mov_b64 exec, s[100:101]
	s_waitcnt vmcnt(0)
	v_lshlrev_b32_e32 v0, 7, v15
	v_and_b32_e32 v0, 0xfffffc00, v0
	v_add_u32_e32 v0, v8, v0
	v_lshlrev_b32_e32 v1, 7, v1
	v_lshlrev_b32_e32 v2, 7, v2
	v_lshlrev_b32_e32 v3, 7, v3
	v_and_b32_e32 v1, 0xfffffc00, v1
	v_and_b32_e32 v2, 0xfffffc00, v2
	v_and_b32_e32 v3, 0xfffffc00, v3
	v_add_u32_e32 v1, v7, v1
	v_add_u32_e32 v2, v8, v2
	v_add_u32_e32 v3, v7, v3
.LBB0_599:
	v_add_u32_e32 v7, 0, v234
	v_add_u32_e32 v249, 0x21800, v7
	s_nor_b64 s[6:7], s[8:9], s[4:5]
	ds_write_b128 v249, v[0:3]
	s_and_saveexec_b64 s[4:5], s[6:7]
	s_cbranch_execz .LBB0_601
	s_mul_hi_u32 s6, s70, 0xaaaaaaab
	s_lshr_b32 s6, s6, 1
	s_mul_i32 s6, s6, 3
	s_sub_i32 s6, s70, s6
	v_lshl_add_u32 v1, s6, 11, v237
	v_mov_b64_e32 v[204:205], s[50:51]
	ds_write2st64_b32 v1, v22, v20 offset1:4
